# FoX epilogue: first output row's gate loads also issued together ahead of its elements (all 16 rows now batched or prefetched); placement kept
# baseline (speedup 1.0000x reference)
; __device__ __forceinline__ unsigned cvt_pk_bf16(float lo, float hi) { unsigned r; asm volatile("v_cvt_pk_bf16_f32 %0, %1, %2" : "=v"(r) : "v"(lo), "v"(hi)); return r; }
; __device__ __forceinline__ float bf_lo(unsigned w) { return __uint_as_float(w << 16); }
; __device__ __forceinline__ float bf_hi(unsigned w) { return __uint_as_float(w & 0xffff0000u); }
; __device__ __forceinline__ int crow(int r, int hi) { return (r & 3) + 8 * (r >> 2) + 4 * hi; }
; template <int MODE> ...
;     ...
;     if (hi == 0) li_l[r32] = l_reg; asm volatile("s_waitcnt lgkmcnt(0)" ::: "memory");
; #pragma unroll
;     for (int r = 0; r < 16; ++r) { const int orow = qlo + crow(r, hi); const float rl = __builtin_amdgcn_rcpf(li_l[crow(r, hi)]);
; #pragma unroll
;         for (int d0 = 0; d0 < 4; ++d0) { float v = o[d0][r] * rl; float vn = __shfl_xor(v, 1);
;             if ((r32 & 1) == 0) { const int col = d0 * 32 + r32;
;                 if (MODE == 1) { const unsigned g = *(const unsigned*)(gate + (size_t)orow * 1024 + hoff + col); v *= bf_lo(g); vn *= bf_hi(g); }
;                 *(unsigned*)(Ob + (size_t)orow * DM + ocol0 + col) = cvt_pk_bf16(v, vn); } } }
.LBB0_1410:
	s_and_saveexec_b64 s[0:1], s[4:5]
	v_readlane_b32 s10, v240, 8
	ds_write_b32 v163, v178
	s_or_b64 exec, exec, s[0:1]
	s_waitcnt lgkmcnt(0)
	ds_read_b32 v5, v160
	v_and_b32_e32 v4, 64, v1
	v_xor_b32_e32 v2, 1, v1
	v_add_u32_e32 v4, 64, v4
	v_cmp_lt_i32_e32 vcc, v2, v4
	s_waitcnt lgkmcnt(0)
	v_rcp_f32_e32 v11, v5
	v_add_u32_e32 v4, s10, v162
	v_cndmask_b32_e32 v2, v1, v2, vcc
	v_lshlrev_b32_e32 v10, 2, v2
	v_mul_f32_e32 v12, v66, v11
	s_nop 1
	v_mov_b32_dpp v13, v12 quad_perm:[1,0,3,2] row_mask:0xf bank_mask:0xf
	v_ashrrev_i32_e32 v5, 31, v4
	v_readlane_b32 s6, v240, 14
	v_lshlrev_b64 v[6:7], 11, v[4:5]
	v_readlane_b32 s7, v240, 15
	v_readlane_b32 s8, v240, 16
	v_readlane_b32 s9, v240, 17
	v_lshl_add_u64 v[8:9], s[6:7], 0, v[6:7]
	v_lshlrev_b64 v[6:7], 12, v[4:5]
	v_lshl_add_u64 v[6:7], s[8:9], 0, v[6:7]
	v_lshlrev_b32_e32 v2, 1, v161
	v_lshl_add_u64 v[252:253], v[8:9], 0, v[2:3]
	global_load_dword v248, v[252:253], off
	global_load_dword v249, v[252:253], off offset:64
	global_load_dword v250, v[252:253], off offset:128
	global_load_dword v251, v[252:253], off offset:192
	s_and_saveexec_b64 s[0:1], s[2:3]
	s_cbranch_execz .LBB0_1414
	v_lshl_add_u64 v[14:15], v[8:9], 0, v[2:3]
	s_waitcnt vmcnt(0)
	v_mov_b32_e32 v5, v248
	v_lshlrev_b32_e32 v14, 16, v5
	v_and_b32_e32 v5, 0xffff0000, v5
	v_mul_f32_e32 v12, v12, v14
	s_waitcnt lgkmcnt(0)
	v_mul_f32_e32 v5, v13, v5
	v_cvt_pk_bf16_f32 v5, v12, v5
	v_lshl_add_u64 v[12:13], v[6:7], 0, v[2:3]
	global_store_dword v[12:13], v5, off
.LBB0_1414:
	s_or_b64 exec, exec, s[0:1]
	v_mul_f32_e32 v5, v50, v11
	s_nop 1
	v_mov_b32_dpp v12, v5 quad_perm:[1,0,3,2] row_mask:0xf bank_mask:0xf
	s_and_saveexec_b64 s[0:1], s[2:3]
	s_cbranch_execz .LBB0_1416
	v_lshl_add_u64 v[14:15], v[8:9], 0, v[2:3]
	s_waitcnt lgkmcnt(0)
	v_mov_b32_e32 v13, v249
	v_lshlrev_b32_e32 v14, 16, v13
	v_and_b32_e32 v13, 0xffff0000, v13
	v_mul_f32_e32 v5, v5, v14
	s_waitcnt lgkmcnt(0)
	v_mul_f32_e32 v12, v12, v13
	v_cvt_pk_bf16_f32 v5, v5, v12
	v_lshl_add_u64 v[12:13], v[6:7], 0, v[2:3]
	global_store_dword v[12:13], v5, off offset:64
.LBB0_1416:
	s_or_b64 exec, exec, s[0:1]
	v_mul_f32_e32 v5, v34, v11
	s_waitcnt lgkmcnt(0)
	s_nop 1
	v_mov_b32_dpp v12, v5 quad_perm:[1,0,3,2] row_mask:0xf bank_mask:0xf
	s_and_saveexec_b64 s[0:1], s[2:3]
	s_cbranch_execz .LBB0_1418
	v_lshl_add_u64 v[14:15], v[8:9], 0, v[2:3]
	v_mov_b32_e32 v13, v250
	v_lshlrev_b32_e32 v14, 16, v13
	v_and_b32_e32 v13, 0xffff0000, v13
	v_mul_f32_e32 v5, v5, v14
	s_waitcnt lgkmcnt(0)
	v_mul_f32_e32 v12, v12, v13
	v_cvt_pk_bf16_f32 v5, v5, v12
	v_lshl_add_u64 v[12:13], v[6:7], 0, v[2:3]
	global_store_dword v[12:13], v5, off offset:128
.LBB0_1418:
	s_or_b64 exec, exec, s[0:1]
	v_mul_f32_e32 v5, v18, v11
	s_nop 1
	v_mov_b32_dpp v11, v5 quad_perm:[1,0,3,2] row_mask:0xf bank_mask:0xf
	s_and_saveexec_b64 s[0:1], s[2:3]
	s_cbranch_execz .LBB0_1420
	v_lshl_add_u64 v[8:9], v[8:9], 0, v[2:3]
	v_lshl_add_u64 v[6:7], v[6:7], 0, v[2:3]
	v_mov_b32_e32 v8, v251
	v_lshlrev_b32_e32 v9, 16, v8
	v_and_b32_e32 v8, 0xffff0000, v8
	v_mul_f32_e32 v5, v5, v9
	s_waitcnt lgkmcnt(0)
	v_mul_f32_e32 v8, v11, v8
	v_cvt_pk_bf16_f32 v5, v5, v8
	global_store_dword v[6:7], v5, off offset:192

; #define PG8_STAGE(bufoff, gbase, voff) do { _Pragma("unroll") for (int _i = 0; _i < 2; ++_i) glds16_s((const void*)((const char*)(gbase) + _i * r64), (voff), ldsb + (unsigned)(bufoff) + ldsw + _i * 8192u); } while (0)
; #define PG8_WAIT_V(n) asm volatile("s_waitcnt vmcnt(" #n ")" ::: "memory")
; #define PG8_BAR __builtin_amdgcn_s_barrier()
; template <class Epi, class Sched, bool FP8 = false>
; __device__ __forceinline__ void gemm_phase(LAS unsigned char* lds, const int Kb, const int nt  , const Sched& S, const Epi& E) {
;     ...
;     PG8_STAGE(PG8_SB(0, 0), cB, voffB); PG8_STAGE(PG8_SA(0, 0), cA, voffA); PG8_STAGE(PG8_SB(0, 1), cB + hstep, voffB); PG8_STAGE(PG8_SA(0, 1), cA + hstep, voffA);
;     if (wr == 1) PG8_BAR;
;     PG8_WAIT_V(4); PG8_BAR;
;     PG8_STAGE(PG8_SB(1, 0), cB + kstep, voffB); PG8_STAGE(PG8_SA(1, 0), cA + kstep, voffA); PG8_STAGE(PG8_SB(1, 1), cB + hstep + kstep, voffB);
;     PG8_WAIT_V(6); PG8_BAR;
.LBB0_1706:
	v_readlane_b32 s4, v241, 5
	v_readlane_b32 s5, v241, 6
	s_add_u32 s4, s4, 0x56f00000
	s_addc_u32 s5, s5, 0
	s_lshl_b32 s3, s3, 5
	s_and_b32 s46, s3, 0x60
	s_lshl_b32 s45, s6, 6
	s_lshl_b32 s8, s6, 13
	s_lshl_b32 s3, s46, 7
	s_add_u32 s6, s24, 0x80
	s_addc_u32 s7, s25, 0
	s_add_i32 s47, s37, 0x18000
	s_waitcnt vmcnt(4)
	s_barrier
	s_mov_b32 s9, m0
	s_mov_b32 m0, s47
	s_nop 0
	global_load_lds_dwordx4 v1, s[6:7]
	s_mov_b32 m0, s9
	s_add_u32 s6, s24, 0x40080
	s_addc_u32 s7, s25, 0
	s_add_i32 s48, s37, 0x1a000
	s_mov_b32 s9, m0
	s_mov_b32 m0, s48
	s_nop 0
	global_load_lds_dwordx4 v1, s[6:7]
	s_mov_b32 m0, s9
	s_add_u32 s6, s22, 0x80
	s_addc_u32 s7, s23, 0
	s_add_i32 s49, s37, 0x8000
	s_mov_b32 s9, m0
	s_mov_b32 m0, s49
	s_nop 0
	global_load_lds_dwordx4 v1, s[6:7]
	s_mov_b32 m0, s9
	s_add_u32 s6, s22, 0x40080
	s_addc_u32 s7, s23, 0
	s_add_i32 s50, s37, 0xa000
	s_mov_b32 s9, m0
	s_mov_b32 m0, s50
	s_nop 0
	global_load_lds_dwordx4 v1, s[6:7]
	s_mov_b32 m0, s9
	s_add_u32 s6, s24, 0x80080
	s_addc_u32 s7, s25, 0
	s_add_i32 s51, s37, 0x1c000
	v_lshlrev_b32_e32 v3, 6, v0
	v_lshlrev_b32_e32 v4, 2, v0
	s_mov_b32 s9, m0
	s_mov_b32 m0, s51
	s_nop 0
	global_load_lds_dwordx4 v1, s[6:7]
	s_mov_b32 m0, s9
	s_add_u32 s6, s24, 0xc0080
	v_and_b32_e32 v2, 48, v0
	v_and_b32_e32 v3, 0x3c0, v3
	v_and_b32_e32 v4, 32, v4
	s_addc_u32 s7, s25, 0
	s_add_i32 s52, s37, 0x1e000
	s_mov_b32 s9, m0
	s_mov_b32 m0, s52
	s_nop 0
	global_load_lds_dwordx4 v1, s[6:7]
	s_mov_b32 m0, s9
	v_bitop3_b32 v2, v3, v4, v2 bitop3:0x36
	s_waitcnt vmcnt(6)
	s_add_i32 s3, s3, 0
	s_add_i32 s53, s37, 0xc000
	s_add_i32 s54, s37, 0xe000
	v_add_u32_e32 v3, s3, v2
	v_add_u32_e32 v2, 0, v2
	s_cmp_lg_u64 s[76:77], 0
	s_waitcnt vmcnt(5)
	v_add_u32_e32 v138, 0x10000, v3
	v_add_u32_e32 v139, 0x10400, v3
	v_add_u32_e32 v140, 0x10800, v3
	v_add_u32_e32 v141, 0x10c00, v3
	s_waitcnt vmcnt(4)
	v_add_u32_e32 v142, 0x14000, v3
	v_add_u32_e32 v143, 0x14400, v3
	v_add_u32_e32 v144, 0x14800, v3
	v_add_u32_e32 v145, 0x14c00, v3
	s_waitcnt vmcnt(0)
	v_add_u32_e32 v146, 0x18000, v3
	v_add_u32_e32 v147, 0x18400, v3
	v_add_u32_e32 v148, 0x18800, v3
	v_add_u32_e32 v149, 0x18c00, v3
	v_add_u32_e32 v150, 0x1c000, v3
	v_add_u32_e32 v151, 0x1c400, v3
	v_add_u32_e32 v152, 0x1c800, v3
	v_add_u32_e32 v153, 0x1cc00, v3
	s_cselect_b64 s[6:7], -1, 0
	v_add_u32_e32 v154, s8, v2
	s_mov_b64 s[8:9], 0x48000
	s_mov_b64 s[10:11], 0x50000
	s_mov_b64 s[12:13], 0x58000
	s_mov_b64 s[18:19], s[22:23]
	s_mov_b64 s[20:21], s[24:25]
	s_barrier
	s_branch .LBB0_1708
	s_nop 0
	s_nop 0
	s_nop 0
	s_nop 0
	s_nop 0
	s_nop 0
	s_nop 0
	s_nop 0
	s_nop 0
	s_nop 0
	s_nop 0
	s_nop 0
.LBB0_1707:
	global_store_dwordx4 v[20:21], v[2:5], off offset:576
